# v74 plus window attention: the 16 serialized distance-table reads of a round (one LDS round trip each) issued as one batch into fresh registers ahead of the fragment reads
# speedup vs baseline: 1.0035x; 1.0035x over previous
;     ...
;                 if (MODE != 3) {
; #pragma unroll
;                     for (int kt = 0; kt < 4; ++kt)
; #pragma unroll
;                         for (int ks = 0; ks < 2; ++ks) akf[kt][ks] = *(const LAS bf16x8*)(L + LK + (16 * kt + n) * 128 + ((((4 * ks + q) ^ n) & 7) << 4));
;                     if (do_pv) {
; #pragma unroll
;                         for (int st = 0; st < 2; ++st)
; #pragma unroll
;                             for (int dt = 0; dt < 4; ++dt) avf[st][dt] = *(const LAS bf16x8*)(L + LV + (16 * dt + n) * 128 + ((((4 * st + q) ^ n) & 7) << 4)); }
;     ...
; #pragma unroll
;                         for (int kt = 0; kt < 4; ++kt) { sc[kt] = (f32x4){0.f, 0.f, 0.f, 0.f};
; #pragma unroll
;                             for (int ks = 0; ks < 2; ++ks) { const bf16x8 ak = (MODE != 3) ? akf[kt][ks] : akq[kt][ks];
;                                 sc[kt] = __builtin_amdgcn_mfma_f32_16x16x32_bf16(ak, Bq[qd][ks], sc[kt], 0, 0, 0); } }
;                         if (MODE == 3) {
; #pragma unroll
;                             for (int st = 0; st < 2; ++st)
; #pragma unroll
;                                 for (int dt = 0; dt < 4; ++dt) avq[st][dt] = *(const LAS bf16x8*)(L + LV + (16 * dt + n) * 128 + ((((4 * st + q) ^ n) & 7) << 4));
;                             __builtin_amdgcn_sched_barrier(0);
;                         }
;                         if (!far) {
;                             const LAS float* tp = (MODE == 2) ? biasd + hr * NT + (DOFF - tq + 31 + 16 * p0) + 64 * q : biasd + hr * NT + (DOFF - tq + p0) + 4 * q;
; #pragma unroll
;                             for (int kt = 0; kt < 4; ++kt)
; #pragma unroll
;                                 for (int r = 0; r < 4; ++r) sc[kt][r] += (MODE == 3) ? bia[kt][r] : ((MODE == 2) ? tp[256 * kt + 16 * r] : tp[16 * kt + r]);
;                         }
;                         const float bshift = far ? bfar : 0.f, boff = bshift * 1.4426950408889634f;
;                         float mx;
;                         { float m = fmaxf(fmaxf(sc[0][0], sc[0][1]), sc[0][2]);
;                           m = fmaxf(fmaxf(m, sc[0][3]), sc[1][0]); m = fmaxf(fmaxf(m, sc[1][1]), sc[1][2]); m = fmaxf(fmaxf(m, sc[1][3]), sc[2][0]);
;                           m = fmaxf(fmaxf(m, sc[2][1]), sc[2][2]); m = fmaxf(fmaxf(m, sc[2][3]), sc[3][0]); m = fmaxf(fmaxf(m, sc[3][1]), sc[3][2]); mx = fmaxf(m, sc[3][3]) + bshift; }
.LBB0_1047:
	s_mov_b32 s9, s7
	s_add_i32 s7, s7, 64
	s_add_i32 s42, s7, 64
	s_max_i32 s42, s42, 0
	s_lshl_b64 s[10:11], s[42:43], 13
	s_lshl_b32 s42, s42, 1
	s_waitcnt lgkmcnt(0)
	s_barrier
	s_waitcnt vmcnt(3)
	ds_write_b128 v153, v[54:57]
	s_waitcnt vmcnt(2)
	ds_write_b64 v154, v[50:51] offset:8192
	ds_write_b64 v155, v[52:53] offset:8192
	v_lshl_add_u64 v[50:51], v[138:139], 0, s[10:11]
	v_lshl_add_u64 v[52:53], v[140:141], 0, s[42:43]
	global_load_dwordx4 v[54:57], v[50:51], off
	s_nop 0
	global_load_dwordx4 v[50:53], v[52:53], off
	s_cmp_lt_i32 s9, 0
	s_cselect_b64 s[10:11], -1, 0
	s_cmp_gt_i32 s9, s13
	s_cselect_b64 s[14:15], -1, 0
	s_add_i32 s9, s9, 63
	s_cmp_lt_i32 s9, s12
	s_cselect_b64 s[16:17], -1, 0
	s_or_b64 s[10:11], s[10:11], s[16:17]
	s_or_b64 s[10:11], s[10:11], s[14:15]
	s_and_b64 vcc, exec, s[10:11]
	s_waitcnt lgkmcnt(0)
	s_barrier
	s_cbranch_vccnz .LBB0_1046
	v_add_u32_e32 v208, s8, v152
	v_add_u32_e32 v209, 0x207ec, v208
	ds_read2_b32 v[210:211], v209 offset0:4 offset1:5
	ds_read2_b32 v[212:213], v209 offset0:6 offset1:7
	ds_read2_b32 v[214:215], v209 offset0:20 offset1:21
	ds_read2_b32 v[216:217], v209 offset0:22 offset1:23
	ds_read2_b32 v[218:219], v209 offset0:36 offset1:37
	ds_read2_b32 v[220:221], v209 offset0:38 offset1:39
	ds_read2_b32 v[222:223], v209 offset0:52 offset1:53
	ds_read2_b32 v[224:225], v209 offset0:54 offset1:55
	ds_read2_b32 v[226:227], v209 offset1:1
	ds_read2_b32 v[228:229], v209 offset0:2 offset1:3
	ds_read2_b32 v[230:231], v209 offset0:16 offset1:17
	ds_read2_b32 v[232:233], v209 offset0:18 offset1:19
	ds_read2_b32 v[236:237], v209 offset0:32 offset1:33
	ds_read2_b32 v[238:239], v209 offset0:34 offset1:35
	ds_read2_b32 v[240:241], v209 offset0:48 offset1:49
	ds_read2_b32 v[242:243], v209 offset0:50 offset1:51
	v_add_u32_e32 v58, v143, v147
	ds_read_b128 v[90:93], v58
	v_add_u32_e32 v59, v143, v148
	ds_read_b128 v[94:97], v59
	ds_read_b128 v[98:101], v58 offset:2048
	ds_read_b128 v[102:105], v59 offset:2048
	ds_read_b128 v[106:109], v58 offset:4096
	ds_read_b128 v[110:113], v59 offset:4096
	ds_read_b128 v[114:117], v58 offset:6144
	ds_read_b128 v[118:121], v59 offset:6144
	ds_read_b128 v[86:89], v58 offset:8192
	ds_read_b128 v[82:85], v58 offset:10240
	ds_read_b128 v[78:81], v58 offset:12288
	ds_read_b128 v[74:77], v58 offset:14336
	ds_read_b128 v[70:73], v59 offset:8192
	ds_read_b128 v[66:69], v59 offset:10240
	ds_read_b128 v[62:65], v59 offset:12288
	ds_read_b128 v[58:61], v59 offset:14336
	s_waitcnt lgkmcnt(13)
	v_mfma_f32_16x16x32_bf16 v[164:167], v[98:101], v[42:45], 0
	s_waitcnt lgkmcnt(12)
	v_mfma_f32_16x16x32_bf16 v[164:167], v[102:105], v[46:49], v[164:167]
	v_mfma_f32_16x16x32_bf16 v[158:161], v[90:93], v[42:45], 0
	v_mfma_f32_16x16x32_bf16 v[160:163], v[94:97], v[46:49], v[158:161]
	s_waitcnt lgkmcnt(11)
	v_mfma_f32_16x16x32_bf16 v[168:171], v[106:109], v[42:45], 0
	s_nop 4
	v_add_u32_e32 v158, s8, v152
	s_waitcnt lgkmcnt(11)
	v_mfma_f32_16x16x32_bf16 v[168:171], v[110:113], v[46:49], v[168:171]
	s_waitcnt lgkmcnt(0)
	v_add_f32_e32 v159, v160, v210
	v_add_f32_e32 v160, v161, v211
	v_mfma_f32_16x16x32_bf16 v[172:175], v[114:117], v[42:45], 0
	s_waitcnt lgkmcnt(0)
	v_add_f32_e32 v161, v162, v212
	v_add_f32_e32 v162, v163, v213
	v_mfma_f32_16x16x32_bf16 v[172:175], v[118:121], v[46:49], v[172:175]
	s_waitcnt lgkmcnt(0)
	v_add_f32_e32 v163, v164, v214
	v_add_f32_e32 v164, v165, v215
	s_waitcnt lgkmcnt(0)
	v_add_f32_e32 v165, v166, v216
	v_add_f32_e32 v166, v167, v217
	s_waitcnt lgkmcnt(0)
	v_add_f32_e32 v167, v168, v218
	v_add_f32_e32 v168, v169, v219
	s_waitcnt lgkmcnt(0)
	v_add_f32_e32 v169, v170, v220
	v_add_f32_e32 v170, v171, v221
	s_waitcnt lgkmcnt(0)
	v_add_f32_e32 v171, v172, v222
	v_add_f32_e32 v172, v173, v223
	s_waitcnt lgkmcnt(0)
	v_add_f32_e32 v173, v174, v224
	v_add_f32_e32 v174, v175, v225
	v_max_f32_e32 v175, v159, v160
	v_max3_f32 v175, v175, v161, v162
	v_max3_f32 v175, v175, v163, v164
	v_max3_f32 v175, v175, v165, v166
	v_max3_f32 v175, v175, v167, v168
	v_max3_f32 v175, v175, v169, v170
	v_max3_f32 v175, v175, v171, v172
	v_max3_f32 v175, v175, v173, v174
	v_add_f32_e32 v176, 0x40c00000, v157
	v_cmp_gt_f32_e32 vcc, v175, v176
	s_cbranch_vccz .LBB0_1050
	v_add_f32_e32 v175, 0, v175
	ds_bpermute_b32 v176, v144, v175
	s_waitcnt lgkmcnt(0)
	v_max_f32_e32 v176, v176, v176
	v_max_f32_e32 v175, v175, v176
	ds_bpermute_b32 v176, v145, v175
	s_waitcnt lgkmcnt(0)
	v_max3_f32 v175, v157, v175, v176
	v_sub_f32_e32 v157, v157, v175
	v_mul_f32_e32 v157, 0x3fb8aa3b, v157
	v_exp_f32_e32 v176, v157
	v_mov_b32_e32 v157, v175
	v_mul_f32_e32 v137, v137, v176
	v_pk_mul_f32 v[32:33], v[32:33], v[176:177] op_sel_hi:[1,0]
	v_pk_mul_f32 v[30:31], v[30:31], v[176:177] op_sel_hi:[1,0]
	v_pk_mul_f32 v[28:29], v[28:29], v[176:177] op_sel_hi:[1,0]
	v_pk_mul_f32 v[26:27], v[26:27], v[176:177] op_sel_hi:[1,0]
	v_pk_mul_f32 v[24:25], v[24:25], v[176:177] op_sel_hi:[1,0]
	v_pk_mul_f32 v[22:23], v[22:23], v[176:177] op_sel_hi:[1,0]
	v_pk_mul_f32 v[20:21], v[20:21], v[176:177] op_sel_hi:[1,0]
	v_pk_mul_f32 v[18:19], v[18:19], v[176:177] op_sel_hi:[1,0]
.LBB0_1050:
	v_mfma_f32_16x16x32_bf16 v[90:93], v[90:93], v[34:37], 0
	v_fma_f32 v175, v157, s24, 0
	v_cmp_ngt_f32_e32 vcc, s30, v157
	v_mfma_f32_16x16x32_bf16 v[92:95], v[94:97], v[38:41], v[90:93]
	s_nop 0
	v_cndmask_b32_e32 v175, 0, v175, vcc
	v_fmamk_f32 v159, v159, 0x3fb8aa3b, v175
	v_fmamk_f32 v160, v160, 0x3fb8aa3b, v175
	v_mfma_f32_16x16x32_bf16 v[96:99], v[98:101], v[34:37], 0
	v_fmamk_f32 v161, v161, 0x3fb8aa3b, v175
	v_fmamk_f32 v162, v162, 0x3fb8aa3b, v175
	v_mfma_f32_16x16x32_bf16 v[98:101], v[102:105], v[38:41], v[96:99]
	v_fmamk_f32 v163, v163, 0x3fb8aa3b, v175
	v_fmamk_f32 v164, v164, 0x3fb8aa3b, v175
	v_fmamk_f32 v165, v165, 0x3fb8aa3b, v175
	s_nop 0
	v_mfma_f32_16x16x32_bf16 v[102:105], v[106:109], v[34:37], 0
	v_fmamk_f32 v166, v166, 0x3fb8aa3b, v175
	v_exp_f32_e32 v159, v159
	v_exp_f32_e32 v160, v160
	s_waitcnt lgkmcnt(0)
	v_add_f32_e32 v91, v92, v226
	v_add_f32_e32 v90, v93, v227
	v_mfma_f32_16x16x32_bf16 v[102:105], v[110:113], v[38:41], v[102:105]
	v_exp_f32_e32 v161, v161
	v_exp_f32_e32 v162, v162
	v_exp_f32_e32 v163, v163
	s_waitcnt lgkmcnt(0)
	v_add_f32_e32 v93, v94, v228
	v_add_f32_e32 v92, v95, v229
	v_mfma_f32_16x16x32_bf16 v[106:109], v[114:117], v[34:37], 0
	v_exp_f32_e32 v164, v164
	v_exp_f32_e32 v165, v165
	v_exp_f32_e32 v166, v166
	s_waitcnt lgkmcnt(0)
	v_add_f32_e32 v95, v98, v230
	v_add_f32_e32 v94, v99, v231
	v_mfma_f32_16x16x32_bf16 v[106:109], v[118:121], v[38:41], v[106:109]
	v_fmamk_f32 v167, v167, 0x3fb8aa3b, v175
	v_fmamk_f32 v168, v168, 0x3fb8aa3b, v175
	v_fmamk_f32 v169, v169, 0x3fb8aa3b, v175
	s_waitcnt lgkmcnt(0)
	v_add_f32_e32 v99, v100, v232
	v_add_f32_e32 v98, v101, v233
	v_fmamk_f32 v170, v170, 0x3fb8aa3b, v175
	v_fmamk_f32 v171, v171, 0x3fb8aa3b, v175
	v_fmamk_f32 v172, v172, 0x3fb8aa3b, v175
	v_fmamk_f32 v173, v173, 0x3fb8aa3b, v175
	s_waitcnt lgkmcnt(0)
	v_add_f32_e32 v101, v102, v236
	v_add_f32_e32 v100, v103, v237
	v_fmac_f32_e32 v175, 0x3fb8aa3b, v174
	v_exp_f32_e32 v167, v167
	v_exp_f32_e32 v168, v168
	v_exp_f32_e32 v169, v169
	s_waitcnt lgkmcnt(0)
	v_add_f32_e32 v103, v104, v238
	v_add_f32_e32 v102, v105, v239
	v_exp_f32_e32 v170, v170
	v_exp_f32_e32 v171, v171
	v_exp_f32_e32 v172, v172
	v_exp_f32_e32 v173, v173
	s_waitcnt lgkmcnt(0)
	v_add_f32_e32 v97, v106, v240
	v_add_f32_e32 v96, v107, v241
	v_exp_f32_e32 v174, v175
	v_cvt_pk_bf16_f32 v180, v159, v160
	v_cvt_pk_bf16_f32 v181, v161, v162
	v_cvt_pk_bf16_f32 v182, v163, v164
	v_cvt_pk_bf16_f32 v183, v165, v166
	s_waitcnt lgkmcnt(0)
	v_add_f32_e32 v105, v108, v242
	v_max_f32_e32 v106, v91, v90
	v_mfma_f32_16x16x32_bf16 v[30:33], v[86:89], v[180:183], v[30:33]
	v_max3_f32 v106, v106, v93, v92
	v_max3_f32 v106, v106, v95, v94
	v_max3_f32 v106, v106, v99, v98
	v_mfma_f32_16x16x32_bf16 v[26:29], v[82:85], v[180:183], v[26:29]
	v_max3_f32 v106, v106, v101, v100
	v_max3_f32 v106, v106, v103, v102
	v_add_f32_e32 v104, v109, v243
	v_mfma_f32_16x16x32_bf16 v[22:25], v[78:81], v[180:183], v[22:25]
	v_max3_f32 v106, v106, v97, v96
	v_max3_f32 v106, v106, v105, v104
	v_add_f32_e32 v107, 0x40c00000, v131
	v_mfma_f32_16x16x32_bf16 v[18:21], v[74:77], v[180:183], v[18:21]
	v_cvt_pk_bf16_f32 v180, v167, v168
	v_cvt_pk_bf16_f32 v181, v169, v170
	v_cvt_pk_bf16_f32 v182, v171, v172
	v_cvt_pk_bf16_f32 v183, v173, v174
	v_cmp_gt_f32_e32 vcc, v106, v107
	s_nop 0
	v_mfma_f32_16x16x32_bf16 v[30:33], v[70:73], v[180:183], v[30:33]
	v_mfma_f32_16x16x32_bf16 v[26:29], v[66:69], v[180:183], v[26:29]
	v_mfma_f32_16x16x32_bf16 v[22:25], v[62:65], v[180:183], v[22:25]
	v_mfma_f32_16x16x32_bf16 v[18:21], v[58:61], v[180:183], v[18:21]
	s_cbranch_vccz .LBB0_1045
	v_add_f32_e32 v106, 0, v106
	ds_bpermute_b32 v107, v144, v106
	s_waitcnt lgkmcnt(0)
	v_max_f32_e32 v107, v107, v107
	v_max_f32_e32 v106, v106, v107
	ds_bpermute_b32 v107, v145, v106
	s_waitcnt lgkmcnt(0)
	v_max3_f32 v107, v131, v106, v107
	v_sub_f32_e32 v106, v131, v107
	v_mul_f32_e32 v106, 0x3fb8aa3b, v106
	v_exp_f32_e32 v106, v106
	v_mov_b32_e32 v131, v107
	v_mul_f32_e32 v136, v136, v106
	v_pk_mul_f32 v[16:17], v[16:17], v[106:107] op_sel_hi:[1,0]
	v_pk_mul_f32 v[14:15], v[14:15], v[106:107] op_sel_hi:[1,0]
	v_pk_mul_f32 v[12:13], v[12:13], v[106:107] op_sel_hi:[1,0]
	v_pk_mul_f32 v[10:11], v[10:11], v[106:107] op_sel_hi:[1,0]
	v_pk_mul_f32 v[8:9], v[8:9], v[106:107] op_sel_hi:[1,0]
	v_pk_mul_f32 v[6:7], v[6:7], v[106:107] op_sel_hi:[1,0]
	v_pk_mul_f32 v[4:5], v[4:5], v[106:107] op_sel_hi:[1,0]
	v_pk_mul_f32 v[2:3], v[2:3], v[106:107] op_sel_hi:[1,0]
	s_branch .LBB0_1045

.Lw2_1047:
	s_mov_b32 s9, s7
	s_add_i32 s7, s7, 64
	s_cmpk_eq_i32 s8, 0x700
	s_cselect_b32 s10, 0, 64
	s_add_i32 s42, s7, s10
	s_max_i32 s42, s42, 0
	s_lshl_b64 s[10:11], s[42:43], 13
	s_lshl_b32 s42, s42, 1
	s_waitcnt lgkmcnt(0)
	s_barrier
	s_waitcnt vmcnt(3)
	ds_write_b128 v153, v[204:207]
	s_waitcnt vmcnt(2)
	ds_write_b64 v154, v[200:201] offset:8192
	ds_write_b64 v155, v[202:203] offset:8192
	v_lshl_add_u64 v[200:201], v[138:139], 0, s[10:11]
	v_lshl_add_u64 v[202:203], v[140:141], 0, s[42:43]
	global_load_dwordx4 v[204:207], v[200:201], off
	s_nop 0
	global_load_dwordx4 v[200:203], v[202:203], off
	s_cmp_lt_i32 s9, 0
	s_cselect_b64 s[10:11], -1, 0
	s_cmp_gt_i32 s9, s13
	s_cselect_b64 s[14:15], -1, 0
	s_add_i32 s9, s9, 63
	s_cmp_lt_i32 s9, s12
	s_cselect_b64 s[16:17], -1, 0
	s_or_b64 s[10:11], s[10:11], s[16:17]
	s_or_b64 s[10:11], s[10:11], s[14:15]
	s_and_b64 vcc, exec, s[10:11]
	s_waitcnt lgkmcnt(0)
	s_barrier
	s_cbranch_vccnz .Lw2_1046
	v_add_u32_e32 v208, s8, v152
	v_add_u32_e32 v209, 0x207ec, v208
	ds_read2_b32 v[210:211], v209 offset0:4 offset1:5
	ds_read2_b32 v[212:213], v209 offset0:6 offset1:7
	ds_read2_b32 v[214:215], v209 offset0:20 offset1:21
	ds_read2_b32 v[216:217], v209 offset0:22 offset1:23
	ds_read2_b32 v[218:219], v209 offset0:36 offset1:37
	ds_read2_b32 v[220:221], v209 offset0:38 offset1:39
	ds_read2_b32 v[222:223], v209 offset0:52 offset1:53
	ds_read2_b32 v[224:225], v209 offset0:54 offset1:55
	ds_read2_b32 v[226:227], v209 offset1:1
	ds_read2_b32 v[228:229], v209 offset0:2 offset1:3
	ds_read2_b32 v[230:231], v209 offset0:16 offset1:17
	ds_read2_b32 v[232:233], v209 offset0:18 offset1:19
	ds_read2_b32 v[236:237], v209 offset0:32 offset1:33
	ds_read2_b32 v[238:239], v209 offset0:34 offset1:35
	ds_read2_b32 v[240:241], v209 offset0:48 offset1:49
	ds_read2_b32 v[242:243], v209 offset0:50 offset1:51
	v_add_u32_e32 v58, v143, v147
	ds_read_b128 v[90:93], v58
	v_add_u32_e32 v59, v143, v148
	ds_read_b128 v[94:97], v59
	ds_read_b128 v[98:101], v58 offset:2048
	ds_read_b128 v[102:105], v59 offset:2048
	ds_read_b128 v[106:109], v58 offset:4096
	ds_read_b128 v[110:113], v59 offset:4096
	ds_read_b128 v[114:117], v58 offset:6144
	ds_read_b128 v[118:121], v59 offset:6144
	ds_read_b128 v[86:89], v58 offset:8192
	ds_read_b128 v[82:85], v58 offset:10240
	ds_read_b128 v[78:81], v58 offset:12288
	ds_read_b128 v[74:77], v58 offset:14336
	ds_read_b128 v[70:73], v59 offset:8192
	ds_read_b128 v[66:69], v59 offset:10240
	ds_read_b128 v[62:65], v59 offset:12288
	ds_read_b128 v[58:61], v59 offset:14336
	s_waitcnt lgkmcnt(13)
	v_mfma_f32_16x16x32_bf16 v[164:167], v[98:101], v[42:45], 0
	s_waitcnt lgkmcnt(12)
	v_mfma_f32_16x16x32_bf16 v[164:167], v[102:105], v[46:49], v[164:167]
	v_mfma_f32_16x16x32_bf16 v[158:161], v[90:93], v[42:45], 0
	v_mfma_f32_16x16x32_bf16 v[160:163], v[94:97], v[46:49], v[158:161]
	s_waitcnt lgkmcnt(11)
	v_mfma_f32_16x16x32_bf16 v[168:171], v[106:109], v[42:45], 0
	s_nop 4
	v_add_u32_e32 v158, s8, v152
	s_waitcnt lgkmcnt(11)
	v_mfma_f32_16x16x32_bf16 v[168:171], v[110:113], v[46:49], v[168:171]
	s_waitcnt lgkmcnt(0)
	v_add_f32_e32 v159, v160, v210
	v_add_f32_e32 v160, v161, v211
	v_mfma_f32_16x16x32_bf16 v[172:175], v[114:117], v[42:45], 0
	s_waitcnt lgkmcnt(0)
	v_add_f32_e32 v161, v162, v212
	v_add_f32_e32 v162, v163, v213
	v_mfma_f32_16x16x32_bf16 v[172:175], v[118:121], v[46:49], v[172:175]
	s_waitcnt lgkmcnt(0)
	v_add_f32_e32 v163, v164, v214
	v_add_f32_e32 v164, v165, v215
	s_waitcnt lgkmcnt(0)
	v_add_f32_e32 v165, v166, v216
	v_add_f32_e32 v166, v167, v217
	s_waitcnt lgkmcnt(0)
	v_add_f32_e32 v167, v168, v218
	v_add_f32_e32 v168, v169, v219
	s_waitcnt lgkmcnt(0)
	v_add_f32_e32 v169, v170, v220
	v_add_f32_e32 v170, v171, v221
	s_waitcnt lgkmcnt(0)
	v_add_f32_e32 v171, v172, v222
	v_add_f32_e32 v172, v173, v223
	s_waitcnt lgkmcnt(0)
	v_add_f32_e32 v173, v174, v224
	v_add_f32_e32 v174, v175, v225
	v_max_f32_e32 v175, v159, v160
	v_max3_f32 v175, v175, v161, v162
	v_max3_f32 v175, v175, v163, v164
	v_max3_f32 v175, v175, v165, v166
	v_max3_f32 v175, v175, v167, v168
	v_max3_f32 v175, v175, v169, v170
	v_max3_f32 v175, v175, v171, v172
	v_max3_f32 v175, v175, v173, v174
	v_add_f32_e32 v176, 0x40c00000, v157
	v_cmp_gt_f32_e32 vcc, v175, v176
	s_cbranch_vccz .Lw2_1050
	v_add_f32_e32 v175, 0, v175
	ds_bpermute_b32 v176, v144, v175
	s_waitcnt lgkmcnt(0)
	v_max_f32_e32 v176, v176, v176
	v_max_f32_e32 v175, v175, v176
	ds_bpermute_b32 v176, v145, v175
	s_waitcnt lgkmcnt(0)
	v_max3_f32 v175, v157, v175, v176
	v_sub_f32_e32 v157, v157, v175
	v_mul_f32_e32 v157, 0x3fb8aa3b, v157
	v_exp_f32_e32 v176, v157
	v_mov_b32_e32 v157, v175
	v_mul_f32_e32 v137, v137, v176
	v_pk_mul_f32 v[32:33], v[32:33], v[176:177] op_sel_hi:[1,0]
	v_pk_mul_f32 v[30:31], v[30:31], v[176:177] op_sel_hi:[1,0]
	v_pk_mul_f32 v[28:29], v[28:29], v[176:177] op_sel_hi:[1,0]
	v_pk_mul_f32 v[26:27], v[26:27], v[176:177] op_sel_hi:[1,0]
	v_pk_mul_f32 v[24:25], v[24:25], v[176:177] op_sel_hi:[1,0]
	v_pk_mul_f32 v[22:23], v[22:23], v[176:177] op_sel_hi:[1,0]
	v_pk_mul_f32 v[20:21], v[20:21], v[176:177] op_sel_hi:[1,0]
	v_pk_mul_f32 v[18:19], v[18:19], v[176:177] op_sel_hi:[1,0]
